# baseline (speedup 1.0000x reference)
.LBB1_4:
	s_or_b64 exec, exec, s[4:5]
	s_mov_b32 s24, s2
	s_ashr_i32 s25, s2, 31
	s_lshl_b64 s[24:25], s[24:25], 15
	s_waitcnt lgkmcnt(0)
	s_add_u32 s24, s12, s24
	s_addc_u32 s25, s13, s25
	v_lshlrev_b32_e32 v52, 4, v0
	global_load_dwordx4 v[56:59], v52, s[24:25] nt
	v_or_b32_e32 v53, 0x400, v0
	v_lshlrev_b32_e32 v53, 4, v53
	global_load_dwordx4 v[60:63], v53, s[24:25] nt
	s_movk_i32 s0, 0x100
	v_sub_u32_e64 v1, s0, v0 clamp
	v_add_u32_e32 v1, 0x3ff, v1
	v_lshrrev_b32_e32 v2, 10, v1
	v_or_b32_e32 v1, 0x400, v0
	v_cmp_ne_u32_e32 vcc, 0, v2
	v_mul_u32_u24_e32 v2, 0x199a, v0
	v_lshrrev_b32_e32 v4, 16, v2
	v_mul_u32_u24_e32 v2, 0x199a, v1
	v_lshrrev_b32_e32 v2, 16, v2
	v_mad_i32_i24 v3, v2, -10, v1
	v_mad_i32_i24 v5, v4, -10, v0
	v_add_u32_e32 v6, 0x80, v3
	v_cmp_gt_i32_e64 s[0:1], 4, v3
	v_add_u32_e32 v7, 0x80, v5
	s_mov_b64 s[4:5], -1
	v_cndmask_b32_e64 v3, v6, v3, s[0:1]
	v_cmp_gt_i32_e64 s[0:1], 4, v5
	s_nop 1
	v_cndmask_b32_e64 v5, v7, v5, s[0:1]
	s_and_saveexec_b64 s[0:1], s[4:5]
	v_mul_u32_u24_e32 v4, 0x228, v4
	v_lshl_add_u32 v4, v5, 2, v4
	v_mov_b32_e32 v5, 0
	ds_write_b32 v4, v5
	s_or_b64 exec, exec, s[0:1]
	s_and_saveexec_b64 s[0:1], vcc
	v_mul_u32_u24_e32 v2, 0x228, v2
	v_lshl_add_u32 v2, v3, 2, v2
	v_mov_b32_e32 v3, 0
	ds_write_b32 v2, v3
	s_or_b64 exec, exec, s[0:1]
	v_sub_u32_e64 v2, 48, v0 clamp
	v_add_u32_e32 v2, 0x3ff, v2
	v_lshrrev_b32_e32 v2, 10, v2
	s_movk_i32 s3, 0x217
	v_cmp_ne_u32_e64 s[0:1], 0, v2
	v_mov_b32_e32 v2, 0xfffffde8
	v_cmp_lt_u32_e64 s[6:7], s3, v0
	v_cmp_lt_u32_e32 vcc, s3, v1
	s_movk_i32 s3, 0x10c
	v_cndmask_b32_e64 v3, 0, v2, s[6:7]
	v_cndmask_b32_e32 v2, 0, v2, vcc
	v_add_u32_e32 v2, v2, v1
	v_add_u32_e32 v3, v3, v0
	s_mov_b64 s[16:17], -1
	v_cmp_gt_i32_e64 s[4:5], s3, v2
	v_cmp_gt_i32_e64 s[8:9], s3, v3
	s_and_saveexec_b64 s[14:15], s[16:17]
	s_cbranch_execz .LBB1_10
	v_mul_i32_i24_e32 v4, 0x7a45, v3
	v_lshrrev_b32_e32 v5, 31, v4
	v_ashrrev_i32_e32 v4, 21, v4
	v_add_u16_e32 v4, v4, v5
	v_bfe_i32 v4, v4, 0, 16
	v_add_u32_e32 v5, 0x80, v4
	v_mov_b32_e32 v6, 0x88
	v_cndmask_b32_e64 v5, v5, v4, s[8:9]
	v_cndmask_b32_e64 v6, 0, v6, s[6:7]
	v_add_u32_e32 v5, v5, v6
	v_mul_i32_i24_e32 v5, 0x10c, v5
	v_mul_i32_i24_e32 v4, 0xfffffef4, v4
	v_add_u32_e32 v4, v5, v4
	v_lshlrev_b32_e32 v3, 2, v3
	s_mov_b32 s3, 0x12980
	v_add3_u32 v3, v4, v3, s3
	v_mov_b32_e32 v4, 0
	ds_write_b32 v3, v4

.LBB1_12:
	s_or_b64 exec, exec, s[6:7]
	s_ashr_i32 s3, s2, 31
	s_lshl_b64 s[4:5], s[2:3], 14
	s_lshl_b64 s[0:1], s[2:3], 15
	s_waitcnt lgkmcnt(0)
	s_add_u32 s0, s12, s0
	s_addc_u32 s1, s13, s1
	v_lshlrev_b32_e32 v2, 4, v0
	v_or_b32_e32 v4, 0x400, v0
	v_lshlrev_b32_e32 v2, 4, v4
	v_lshlrev_b32_e32 v5, 5, v0
	v_and_b32_e32 v10, 0x7f, v0
	s_movk_i32 s7, 0x10c
	v_mov_b32_e32 v11, 0x12980
	v_and_b32_e32 v13, 0x1e0, v5
	v_lshrrev_b32_e32 v14, 4, v4
	v_mul_u32_u24_e32 v4, 0x228, v10
	v_mad_u32_u24 v5, v10, s7, v11
	v_lshrrev_b32_e32 v15, 4, v0
	s_movk_i32 s3, 0x228
	v_or_b32_e32 v2, 0xfffffc00, v0
	v_lshrrev_b32_e32 v3, 7, v0
	s_mov_b64 s[0:1], 0
	s_mov_b32 s2, 0x3eaa53cb
	s_mov_b32 s6, 0x3f4e9071
	s_mov_b32 s8, 0x3eeb7510
	s_mov_b32 s12, 0xbe0a4054
	s_mov_b32 s14, 0xbdaefbd6
	s_mov_b32 s16, 0x3d104972
	s_mov_b32 s18, 0x3daefbd6
	s_mov_b32 s20, 0xbeeb7510
	s_mov_b32 s22, 0xbeaa53cb
	v_mad_u32_u24 v26, v15, s3, v13
	v_mad_u32_u24 v13, v14, s3, v13
	s_movk_i32 s3, 0x6ff
	s_waitcnt vmcnt(1)
	v_cvt_f32_f16_e32 v10, v56
	v_cvt_f32_f16_sdwa v11, v56 dst_sel:DWORD dst_unused:UNUSED_PAD src0_sel:WORD_1
	v_cvt_f32_f16_e32 v6, v57
	v_cvt_f32_f16_sdwa v7, v57 dst_sel:DWORD dst_unused:UNUSED_PAD src0_sel:WORD_1
	v_cvt_f32_f16_e32 v20, v58
	v_cvt_f32_f16_sdwa v21, v58 dst_sel:DWORD dst_unused:UNUSED_PAD src0_sel:WORD_1
	v_cvt_f32_f16_e32 v8, v59
	v_cvt_f32_f16_sdwa v9, v59 dst_sel:DWORD dst_unused:UNUSED_PAD src0_sel:WORD_1
	s_waitcnt vmcnt(0)
	v_cvt_f32_f16_e32 v22, v60
	v_cvt_f32_f16_sdwa v23, v60 dst_sel:DWORD dst_unused:UNUSED_PAD src0_sel:WORD_1
	v_cvt_f32_f16_e32 v16, v61
	v_cvt_f32_f16_sdwa v17, v61 dst_sel:DWORD dst_unused:UNUSED_PAD src0_sel:WORD_1
	v_cvt_f32_f16_e32 v24, v62
	v_cvt_f32_f16_sdwa v25, v62 dst_sel:DWORD dst_unused:UNUSED_PAD src0_sel:WORD_1
	v_cvt_f32_f16_e32 v18, v63
	v_cvt_f32_f16_sdwa v19, v63 dst_sel:DWORD dst_unused:UNUSED_PAD src0_sel:WORD_1
	ds_write2_b64 v26, v[10:11], v[6:7] offset0:2 offset1:3
	ds_write2_b64 v26, v[20:21], v[8:9] offset0:4 offset1:5
	ds_write2_b64 v13, v[22:23], v[16:17] offset0:2 offset1:3
	ds_write2_b64 v13, v[24:25], v[18:19] offset0:4 offset1:5
	s_waitcnt lgkmcnt(0)
	s_barrier

	.amdhsa_kernel _Z6k1_mfePKDF16_PKfS2_S2_S2_PDF16_
		.amdhsa_group_segment_fixed_size 149200
		.amdhsa_private_segment_fixed_size 0
		.amdhsa_kernarg_size 48
		.amdhsa_user_sgpr_count 2
		.amdhsa_user_sgpr_dispatch_ptr 0
		.amdhsa_user_sgpr_queue_ptr 0
		.amdhsa_user_sgpr_kernarg_segment_ptr 1
		.amdhsa_user_sgpr_dispatch_id 0
		.amdhsa_user_sgpr_kernarg_preload_length 0
		.amdhsa_user_sgpr_kernarg_preload_offset 0
		.amdhsa_user_sgpr_private_segment_size 0
		.amdhsa_uses_dynamic_stack 0
		.amdhsa_enable_private_segment 0
		.amdhsa_system_sgpr_workgroup_id_x 1
		.amdhsa_system_sgpr_workgroup_id_y 0
		.amdhsa_system_sgpr_workgroup_id_z 0
		.amdhsa_system_sgpr_workgroup_info 0
		.amdhsa_system_vgpr_workitem_id 0
		.amdhsa_next_free_vgpr 97
		.amdhsa_next_free_sgpr 96
		.amdhsa_accum_offset 64
		.amdhsa_reserve_vcc 1
		.amdhsa_float_round_mode_32 0
		.amdhsa_float_round_mode_16_64 0
		.amdhsa_float_denorm_mode_32 3
		.amdhsa_float_denorm_mode_16_64 3
		.amdhsa_dx10_clamp 1
		.amdhsa_ieee_mode 1
		.amdhsa_fp16_overflow 0
		.amdhsa_tg_split 0
		.amdhsa_exception_fp_ieee_invalid_op 0
		.amdhsa_exception_fp_denorm_src 0
		.amdhsa_exception_fp_ieee_div_zero 0
		.amdhsa_exception_fp_ieee_overflow 0
		.amdhsa_exception_fp_ieee_underflow 0
		.amdhsa_exception_fp_ieee_inexact 0
		.amdhsa_exception_int_div_zero 0
	.end_amdhsa_kernel

amdhsa.kernels:
  - .agpr_count:     0
    .args:
      - .actual_access:  read_only
        .address_space:  global
        .offset:         0
        .size:           8
        .value_kind:     global_buffer
      - .actual_access:  read_only
        .address_space:  global
        .offset:         8
        .size:           8
        .value_kind:     global_buffer
      - .actual_access:  read_only
        .address_space:  global
        .offset:         16
        .size:           8
        .value_kind:     global_buffer
      - .actual_access:  read_only
        .address_space:  global
        .offset:         24
        .size:           8
        .value_kind:     global_buffer
      - .actual_access:  write_only
        .address_space:  global
        .offset:         32
        .size:           8
        .value_kind:     global_buffer
      - .actual_access:  write_only
        .address_space:  global
        .offset:         40
        .size:           8
        .value_kind:     global_buffer
      - .actual_access:  write_only
        .address_space:  global
        .offset:         48
        .size:           8
        .value_kind:     global_buffer
      - .actual_access:  read_only
        .address_space:  global
        .offset:         56
        .size:           8
        .value_kind:     global_buffer
      - .actual_access:  read_only
        .address_space:  global
        .offset:         64
        .size:           8
        .value_kind:     global_buffer
      - .actual_access:  read_only
        .address_space:  global
        .offset:         72
        .size:           8
        .value_kind:     global_buffer
      - .actual_access:  read_only
        .address_space:  global
        .offset:         80
        .size:           8
        .value_kind:     global_buffer
      - .actual_access:  read_only
        .address_space:  global
        .offset:         88
        .size:           8
        .value_kind:     global_buffer
      - .actual_access:  read_only
        .address_space:  global
        .offset:         96
        .size:           8
        .value_kind:     global_buffer
      - .actual_access:  read_only
        .address_space:  global
        .offset:         104
        .size:           8
        .value_kind:     global_buffer
      - .actual_access:  write_only
        .address_space:  global
        .offset:         112
        .size:           8
        .value_kind:     global_buffer
    .group_segment_fixed_size: 18176
    .kernarg_segment_align: 8
    .kernarg_segment_size: 120
    .language:       OpenCL C
    .language_version:
      - 2
      - 0
    .max_flat_workgroup_size: 256
    .name:           _Z5k0_lnPKfS0_S0_S0_PDF16_S1_S1_S0_S0_S0_S0_S0_S0_S0_S1_
    .private_segment_fixed_size: 0
    .sgpr_count:     31
    .sgpr_spill_count: 0
    .symbol:         _Z5k0_lnPKfS0_S0_S0_PDF16_S1_S1_S0_S0_S0_S0_S0_S0_S0_S1_.kd
    .uniform_work_group_size: 1
    .uses_dynamic_stack: false
    .vgpr_count:     70
    .vgpr_spill_count: 0
    .wavefront_size: 64
  - .agpr_count:     0
    .args:
      - .actual_access:  read_only
        .address_space:  global
        .offset:         0
        .size:           8
        .value_kind:     global_buffer
      - .actual_access:  read_only
        .address_space:  global
        .offset:         8
        .size:           8
        .value_kind:     global_buffer
      - .actual_access:  read_only
        .address_space:  global
        .offset:         16
        .size:           8
        .value_kind:     global_buffer
      - .actual_access:  read_only
        .address_space:  global
        .offset:         24
        .size:           8
        .value_kind:     global_buffer
      - .actual_access:  read_only
        .address_space:  global
        .offset:         32
        .size:           8
        .value_kind:     global_buffer
      - .actual_access:  write_only
        .address_space:  global
        .offset:         40
        .size:           8
        .value_kind:     global_buffer
    .group_segment_fixed_size: 149200
    .kernarg_segment_align: 8
    .kernarg_segment_size: 48
    .language:       OpenCL C
    .language_version:
      - 2
      - 0
    .max_flat_workgroup_size: 1024
    .name:           _Z6k1_mfePKDF16_PKfS2_S2_S2_PDF16_
    .private_segment_fixed_size: 0
    .sgpr_count:     30
    .sgpr_spill_count: 0
    .symbol:         _Z6k1_mfePKDF16_PKfS2_S2_S2_PDF16_.kd
    .uniform_work_group_size: 1
    .uses_dynamic_stack: false
    .vgpr_count:     64
    .vgpr_spill_count: 0
    .wavefront_size: 64
  - .agpr_count:     0
    .args:
      - .actual_access:  read_only
        .address_space:  global
        .offset:         0
        .size:           8
        .value_kind:     global_buffer
      - .actual_access:  read_only
        .address_space:  global
        .offset:         8
        .size:           8
        .value_kind:     global_buffer
      - .actual_access:  read_only
        .address_space:  global
        .offset:         16
        .size:           8
        .value_kind:     global_buffer
      - .actual_access:  read_only
        .address_space:  global
        .offset:         24
        .size:           8
        .value_kind:     global_buffer
      - .actual_access:  write_only
        .address_space:  global
        .offset:         32
        .size:           8
        .value_kind:     global_buffer
      - .actual_access:  write_only
        .address_space:  global
        .offset:         40
        .size:           8
        .value_kind:     global_buffer
      - .actual_access:  write_only
        .address_space:  global
        .offset:         48
        .size:           8
        .value_kind:     global_buffer
    .group_segment_fixed_size: 71424
    .kernarg_segment_align: 8
    .kernarg_segment_size: 56
    .language:       OpenCL C
    .language_version:
      - 2
      - 0
    .max_flat_workgroup_size: 512
    .name:           _Z5k2_kvPKDF16_S0_S0_S0_PDF16_S1_Pf
    .private_segment_fixed_size: 0
    .sgpr_count:     33
    .sgpr_spill_count: 0
    .symbol:         _Z5k2_kvPKDF16_S0_S0_S0_PDF16_S1_Pf.kd
    .uniform_work_group_size: 1
    .uses_dynamic_stack: false
    .vgpr_count:     114
    .vgpr_spill_count: 0
    .wavefront_size: 64
  - .agpr_count:     0
    .args:
      - .actual_access:  read_only
        .address_space:  global
        .offset:         0
        .size:           8
        .value_kind:     global_buffer
      - .actual_access:  write_only
        .address_space:  global
        .offset:         8
        .size:           8
        .value_kind:     global_buffer
    .group_segment_fixed_size: 1024
    .kernarg_segment_align: 8
    .kernarg_segment_size: 16
    .language:       OpenCL C
    .language_version:
      - 2
      - 0
    .max_flat_workgroup_size: 256
    .name:           _Z9k3_reducePKfPf
    .private_segment_fixed_size: 0
    .sgpr_count:     13
    .sgpr_spill_count: 0
    .symbol:         _Z9k3_reducePKfPf.kd
    .uniform_work_group_size: 1
    .uses_dynamic_stack: false
    .vgpr_count:     50
    .vgpr_spill_count: 0
    .wavefront_size: 64
  - .agpr_count:     0
    .args:
      - .actual_access:  read_only
        .address_space:  global
        .offset:         0
        .size:           8
        .value_kind:     global_buffer
      - .actual_access:  read_only
        .address_space:  global
        .offset:         8
        .size:           8
        .value_kind:     global_buffer
      - .actual_access:  read_only
        .address_space:  global
        .offset:         16
        .size:           8
        .value_kind:     global_buffer
      - .actual_access:  read_only
        .address_space:  global
        .offset:         24
        .size:           8
        .value_kind:     global_buffer
      - .actual_access:  read_only
        .address_space:  global
        .offset:         32
        .size:           8
        .value_kind:     global_buffer
      - .actual_access:  read_only
        .address_space:  global
        .offset:         40
        .size:           8
        .value_kind:     global_buffer
      - .actual_access:  read_only
        .address_space:  global
        .offset:         48
        .size:           8
        .value_kind:     global_buffer
      - .actual_access:  read_only
        .address_space:  global
        .offset:         56
        .size:           8
        .value_kind:     global_buffer
      - .actual_access:  write_only
        .address_space:  global
        .offset:         64
        .size:           8
        .value_kind:     global_buffer
    .group_segment_fixed_size: 74752
    .kernarg_segment_align: 8
    .kernarg_segment_size: 72
    .language:       OpenCL C
    .language_version:
      - 2
      - 0
    .max_flat_workgroup_size: 512
    .name:           _Z8k4_fusedPKfPKDF16_S2_S0_S0_S2_S0_S0_Pf
    .private_segment_fixed_size: 0
    .sgpr_count:     108
    .sgpr_spill_count: 0
    .symbol:         _Z8k4_fusedPKfPKDF16_S2_S0_S0_S2_S0_S0_Pf.kd
    .uniform_work_group_size: 1
    .uses_dynamic_stack: false
    .vgpr_count:     128
    .vgpr_spill_count: 0
    .wavefront_size: 64
